# baseline (speedup 1.0000x reference)
_Z11attn_kernelILi0EEvPKDF16_S1_S1_PKfS3_PfPDF16_:
	s_and_b32 s26, s2, 7
	s_lshl_b32 s26, s26, 2
	s_lshr_b32 s27, s2, 7
	s_add_u32 s26, s26, s27
	s_lshl_b32 s26, s26, 4
	s_bfe_u32 s27, s2, 0x40003
	s_or_b32 s2, s26, s27
	v_readfirstlane_b32 s3, v0
	s_lshr_b32 s14, s3, 6
	s_lshl_b32 s3, s2, 7
	s_lshr_b32 s12, s2, 4
	s_and_b32 s3, s3, 0x780
	s_lshl_b32 s4, s14, 5
	s_mov_b32 s13, 0
	s_load_dwordx4 s[8:11], s[0:1], 0x0
	s_load_dwordx2 s[18:19], s[0:1], 0x10
	s_add_i32 s3, s4, s3
	s_lshl_b64 s[4:5], s[12:13], 11
	s_add_u32 s16, s4, s3
	s_addc_u32 s17, s5, 0
	s_lshl_b64 s[4:5], s[16:17], 7
	v_and_b32_e32 v164, 31, v0
	s_waitcnt lgkmcnt(0)
	s_add_u32 s4, s8, s4
	v_bfe_u32 v72, v0, 5, 1
	s_addc_u32 s5, s9, s5
	s_lshl_b64 s[22:23], s[12:13], 18
	v_lshlrev_b32_e32 v128, 7, v164
	v_mov_b32_e32 v129, 0
	s_add_u32 s8, s10, s22
	v_lshl_add_u64 v[2:3], s[4:5], 0, v[128:129]
	v_lshlrev_b32_e32 v128, 4, v72
	s_addc_u32 s9, s11, s23
	v_lshl_add_u64 v[10:11], v[2:3], 0, v[128:129]
	v_or_b32_e32 v12, 0x100, v0
	v_lshlrev_b32_e32 v128, 4, v0
	v_lshlrev_b32_e32 v44, 4, v12
	global_load_dwordx4 v[2:5], v128, s[8:9]
	global_load_dwordx4 v[6:9], v44, s[8:9]
	v_lshlrev_b32_e32 v79, 3, v0
	s_movk_i32 s4, 0x48
	v_lshrrev_b32_e32 v73, 3, v0
	v_and_b32_e32 v74, 56, v79
	v_lshrrev_b32_e32 v75, 3, v12
	v_mad_u32_u24 v165, v75, s4, v74
	v_mad_u32_u24 v166, v73, s4, v74
	global_load_dwordx4 v[108:111], v[10:11], off
	global_load_dwordx4 v[104:107], v[10:11], off offset:32
	global_load_dwordx4 v[100:103], v[10:11], off offset:64
	global_load_dwordx4 v[96:99], v[10:11], off offset:96
	s_add_u32 s4, s8, 0x2000
	v_lshlrev_b32_e32 v13, 1, v166
	s_addc_u32 s5, s9, 0
	v_lshlrev_b32_e32 v14, 1, v165
	v_lshlrev_b32_e32 v1, 3, v72
	v_mul_u32_u24_e32 v76, 0x48, v164
	v_lshlrev_b32_e32 v80, 3, v12
	v_mov_b32_e32 v45, v129
	s_mov_b32 s15, 1
	v_add_u32_e32 v77, 0x6000, v13
	v_add_u32_e32 v78, 0x6000, v14
	s_waitcnt vmcnt(5)
	ds_write_b128 v13, v[2:5] offset:24576
	s_waitcnt vmcnt(4)
	ds_write_b128 v14, v[6:9] offset:24576
	s_waitcnt lgkmcnt(0)
	s_barrier
	s_load_dwordx4 s[4:7], s[0:1], 0x28
	v_mov_b32_e32 v86, v44
	s_add_u32 s24, s8, 0x2000
	s_addc_u32 s25, s9, 0
	global_load_dwordx4 v[120:123], v128, s[24:25]
	global_load_dwordx4 v[124:127], v44, s[24:25]
	s_add_u32 s24, s24, 0x2000
	s_addc_u32 s25, s25, 0
	v_add_lshl_u32 v3, v1, v76, 1
	v_lshl_add_u64 v[68:69], s[8:9], 0, v[44:45]
	v_lshl_add_u64 v[66:67], s[8:9], 0, v[128:129]
	v_add_u32_e32 v167, 0x6000, v3
	s_lshl_b64 s[20:21], s[12:13], 17
	v_mov_b32_e32 v81, 0
	v_mov_b32_e32 v82, 0
	v_mov_b32_e32 v130, 0
	v_mov_b32_e32 v131, 0
	v_mov_b32_e32 v132, 0
	v_mov_b32_e32 v133, 0
	v_mov_b32_e32 v134, 0
	v_mov_b32_e32 v135, 0
	v_mov_b32_e32 v136, 0
	v_mov_b32_e32 v137, 0
	v_mov_b32_e32 v138, 0
	v_mov_b32_e32 v139, 0
	v_mov_b32_e32 v140, 0
	v_mov_b32_e32 v141, 0
	v_mov_b32_e32 v142, 0
	v_mov_b32_e32 v143, 0
	v_mov_b32_e32 v144, 0
	v_mov_b32_e32 v145, 0
	v_mov_b32_e32 v34, 0xff800000
	v_mov_b32_e32 v35, v34
	v_mov_b32_e32 v36, v34
	v_mov_b32_e32 v37, v34
	v_mov_b32_e32 v38, v34
	v_mov_b32_e32 v39, v34
	v_mov_b32_e32 v40, v34
	v_mov_b32_e32 v41, v34
	v_mov_b32_e32 v42, v34
	v_mov_b32_e32 v43, v34
	v_mov_b32_e32 v44, v34
	v_mov_b32_e32 v45, v34
	v_mov_b32_e32 v46, v34
	v_mov_b32_e32 v47, v34
	v_mov_b32_e32 v48, v34
	v_mov_b32_e32 v49, v34
	v_mov_b32_e32 v50, v34
	v_mov_b32_e32 v51, v34
	v_mov_b32_e32 v52, v34
	v_mov_b32_e32 v53, v34
	v_mov_b32_e32 v54, v34
	v_mov_b32_e32 v55, v34
	v_mov_b32_e32 v56, v34
	v_mov_b32_e32 v57, v34
	v_mov_b32_e32 v58, v34
	v_mov_b32_e32 v59, v34
	v_mov_b32_e32 v60, v34
	v_mov_b32_e32 v61, v34
	v_mov_b32_e32 v62, v34
	v_mov_b32_e32 v63, v34
	v_mov_b32_e32 v64, v34
	v_mov_b32_e32 v65, v34
	s_mov_b32 s11, 0xff800000
	s_mov_b32 s15, 0
	s_waitcnt vmcnt(2) lgkmcnt(0)
